# attention K tile LDS swizzle widened from 3 to 4 XOR bits (removes 2-way bank conflict on the QK^T ds_read_b128)
# speedup vs baseline: 1.2388x; 1.2388x over previous
; #define LAS __attribute__((address_space(3)))
; __device__ __forceinline__ int opaque_tid() { int t = threadIdx.x; asm volatile("" : "+v"(t)); return t; }
; __device__ __forceinline__ int v_rd_base(int lane) { return ((lane & 3) << 3) | (((lane >> 2) & 3) << 6) | (((lane >> 4) & 1) << 5) | (((lane >> 5) & 1) << 8); }
; __device__ __forceinline__ int v_st256(int k, int c) { const int kk = (k & ~0xC) | ((k & 4) << 1) | ((k & 8) >> 1); return ((kk >> 3) * 8 + (c >> 5)) * 512 + ((kk & 7) * 32 + (c & 31)) * 2; }
; #define SLOAD_A(k0) do { const bf16_t* vp_ = Vh + (long)(k0) * LDK + toff; const bf16_t* kp_ = Kh + (long)(k0) * LDK + toff; \
;     sa0 = *(const bf16x8*)kp_; sa1 = *(const bf16x8*)(kp_ + 32L * LDK); sa2 = *(const bf16x8*)vp_; sa3 = *(const bf16x8*)(vp_ + 128); } while (0)
; #define SWRITE_A(b) do { LAS char* vb_ = V_lds + (b) * SHM_V2 + vst00; LAS char* kb_ = K_lds + (b) * SHM_K2 + kst0; \
;     *(LAS bf16x8*)(kb_) = sa0; *(LAS bf16x8*)(kb_ + 8192) = sa1; *(LAS bf16x8*)(vb_) = sa2; *(LAS bf16x8*)(vb_ + 2048) = sa3; } while (0)
; template <int LDQ, int LDK, int LDO>
; __device__ __forceinline__ void attn_body256(const bf16_t* __restrict__ Qb, const bf16_t* __restrict__ Kh, const bf16_t* __restrict__ Vh, float* __restrict__ Ob, int seq, LAS char* lds) {
;   const int tid = opaque_tid(), wid = tid >> 6, lane = tid & 63, r32 = lane & 31, hi = lane >> 5;
;   LAS char* V_lds = lds; LAS char* K_lds = lds + 2 * SHM_V2;
;   LAS float* wsl = (LAS float*)(lds + 2 * SHM_V2 + 2 * SHM_K2) + wid * 64; LAS float* li_l = wsl; LAS float* al_l = wsl + 32;
;   float m_reg = -1e30f, l_reg = 0; f32x16 o[8] = {}; bf16x8 qr[8];
;   const bf16_t* Qw = Qb + (long)(wid * QBLK + r32) * LDQ + hi * 8;
; #pragma unroll
;   for (int d0 = 0; d0 < 8; ++d0) qr[d0] = *(const bf16x8*)(Qw + d0 * 16);
;   const int sr = tid >> 4, sc = (tid & 15) * 8;
;   const int vst00 = v_st256(sr, sc), kst0 = KSWZ(sr, sc * 2);
;   const unsigned toff = (unsigned)(sr * LDK + sc);
;   const int vb0 = (int)(uintptr_t)V_lds + v_rd_base(lane);
;   bf16x8 sa0, sa1, sa2, sa3;
;     ...
;   f32x16 p0, p1; float mn, al; bf16x8 pa0, pa1, pa2, pa3; const int NT = seq / KVBLK;
;   SLOAD_A(0); asm volatile("s_waitcnt vmcnt(0)" ::: "memory"); SWRITE_A(0); SLOAD_B(0); asm volatile("s_waitcnt vmcnt(0)" ::: "memory"); SWRITE_B(0); __syncthreads();
.LBB0_933:
	s_lshl_b64 s[8:9], s[10:11], 1
	s_add_u32 s6, s4, s8
	s_addc_u32 s7, s5, s9
	v_mov_b32_e32 v226, v241
	s_movk_i32 s82, 0xffe0
	v_ashrrev_i32_e32 v17, 1, v241
	v_bfe_u32 v231, v241, 5, 1
	v_bfi_b32 v2, s82, v17, v241
	v_mov_b64_e32 v[4:5], s[6:7]
	s_movk_i32 s6, 0x3080
	v_mad_i64_i32 v[4:5], s[6:7], v2, s6, v[4:5]
	v_lshlrev_b32_e32 v212, 4, v231
	v_mov_b32_e32 v213, v3
	v_lshlrev_b32_e32 v19, 3, v241
	v_lshl_add_u64 v[4:5], v[4:5], 0, v[212:213]
	v_ashrrev_i32_e32 v18, 4, v241
	v_and_b32_e32 v2, 0x78, v19
	s_movk_i32 s6, 0x1840
	global_load_dwordx4 v[164:167], v[4:5], off
	global_load_dwordx4 v[168:171], v[4:5], off offset:32
	global_load_dwordx4 v[172:175], v[4:5], off offset:64
	global_load_dwordx4 v[176:179], v[4:5], off offset:96
	global_load_dwordx4 v[180:183], v[4:5], off offset:128
	global_load_dwordx4 v[184:187], v[4:5], off offset:160
	global_load_dwordx4 v[188:191], v[4:5], off offset:192
	global_load_dwordx4 v[192:195], v[4:5], off offset:224
	v_mad_u64_u32 v[4:5], s[6:7], v18, s6, v[2:3]
	s_add_u32 s10, s16, s8
	v_mov_b32_e32 v5, v3
	s_addc_u32 s11, s17, s9
	v_lshlrev_b64 v[12:13], 1, v[4:5]
	v_lshl_add_u64 v[4:5], s[10:11], 0, v[12:13]
	s_mov_b32 s6, 0x61000
	s_waitcnt vmcnt(10)
	v_add_co_u32_e32 v8, vcc, s6, v4
	v_lshl_add_u64 v[14:15], s[18:19], 0, v[12:13]
	s_nop 0
	v_addc_co_u32_e32 v9, vcc, 0, v5, vcc
	global_load_dwordx4 v[4:7], v[4:5], off
	s_nop 0
	global_load_dwordx4 v[8:11], v[8:9], off
	s_nop 0
	global_load_dwordx4 v[196:199], v[14:15], off
	global_load_dwordx4 v[200:203], v[14:15], off offset:256
	s_waitcnt vmcnt(0)
	v_lshl_add_u64 v[14:15], s[24:25], 0, v[12:13]
	global_load_dwordx4 v[204:207], v[14:15], off
	global_load_dwordx4 v[208:211], v[14:15], off offset:256
	v_and_b32_e32 v15, 0x3fffffc0, v241
	v_lshlrev_b32_e32 v20, 4, v241
	v_and_b32_e32 v214, 0xffffffe0, v17
	v_lshlrev_b32_e32 v17, 1, v18
	v_lshl_add_u32 v232, v15, 2, s64
	v_and_b32_e32 v15, 3, v18
	v_lshrrev_b32_e32 v22, 1, v18
	v_and_b32_e32 v23, 0x7ffff0, v18
	v_bfe_u32 v24, v19, 5, 2
	v_and_b32_e32 v26, 0x70, v20
	v_and_b32_e32 v27, 0x80, v19
	v_or_b32_e32 v26, v26, v27
	v_and_b32_e32 v17, 8, v17
	v_lshlrev_b32_e32 v2, 1, v2
	s_movk_i32 s7, 0x60
	v_lshlrev_b32_e32 v21, 1, v241
	v_lshlrev_b32_e32 v18, 8, v18
	v_and_b32_e32 v25, 0xc0, v20
	v_and_or_b32 v15, v22, 4, v15
	s_add_i32 s6, 0, 0x10000
	v_xor_b32_e32 v215, v212, v26
	v_bitop3_b32 v235, v212, v26, s7 bitop3:0x36
	s_movk_i32 s7, 0x80
	v_or3_b32 v17, v23, v17, v24
	v_and_b32_e32 v20, 48, v2
	v_bitop3_b32 v2, v2, v241, s65 bitop3:0x78
	v_lshrrev_b32_e32 v27, 1, v241
	v_and_b32_e32 v27, 0x80, v27
	v_xor_b32_e32 v2, v2, v27
	v_and_b32_e32 v213, 31, v241
	v_and_b32_e32 v21, 32, v21
	v_bitop3_b32 v236, v212, v26, s7 bitop3:0x36
	s_movk_i32 s7, 0xa0
	v_lshlrev_b32_e32 v15, 6, v15
	v_lshl_add_u32 v16, v17, 9, 0
	v_add3_u32 v240, s6, v2, v18
	s_movk_i32 s11, 0x118
	s_add_u32 s8, s78, s8
	v_and_b32_e32 v14, 63, v241
	v_bitop3_b32 v237, v212, v26, s7 bitop3:0x36
	s_movk_i32 s7, 0xc0
	v_lshl_add_u32 v239, v213, 8, s6
	v_add3_u32 v241, v16, v15, v20
	s_movk_i32 s6, 0xe0
	v_and_or_b32 v2, v19, s11, v21
	s_addc_u32 s9, s79, s9
	v_mov_b32_e32 v16, v3
	v_mov_b32_e32 v17, v3
	v_bitop3_b32 v233, v212, v26, 32 bitop3:0x36
	v_bitop3_b32 v234, v212, v26, 64 bitop3:0x36
	v_bitop3_b32 v238, v212, v26, s7 bitop3:0x36
	v_bitop3_b32 v242, v212, v26, s6 bitop3:0x36
	v_cmp_gt_u32_e64 s[6:7], 32, v14
	v_add3_u32 v244, v25, 0, v2
	v_lshl_add_u64 v[216:217], s[78:79], 0, v[12:13]
	v_lshl_add_u64 v[218:219], s[8:9], 0, v[12:13]
	v_mov_b32_e32 v2, v3
	v_mov_b32_e32 v12, v3
	v_mov_b32_e32 v13, v3
	s_waitcnt vmcnt(5)
	ds_write_b128 v240, v[4:7]
	s_waitcnt vmcnt(4)
	ds_write_b128 v240, v[8:11] offset:8192
	s_waitcnt vmcnt(3)
	ds_write_b128 v241, v[196:199]
	s_waitcnt vmcnt(2)
	ds_write_b128 v241, v[200:203] offset:2048
	s_waitcnt vmcnt(0)
	v_mov_b32_e32 v4, v3
	v_mov_b32_e32 v5, v3
	v_mov_b32_e32 v6, v3
	v_mov_b32_e32 v7, v3
	v_mov_b32_e32 v8, v3
	v_mov_b32_e32 v9, v3
	v_mov_b32_e32 v10, v3
	v_mov_b32_e32 v11, v3
	v_mov_b32_e32 v14, v3
	v_mov_b32_e32 v15, v3
	v_mov_b64_e32 v[130:131], v[16:17]
	v_mov_b64_e32 v[114:115], v[16:17]
	v_mov_b64_e32 v[98:99], v[16:17]
	v_mov_b64_e32 v[82:83], v[16:17]
	v_mov_b64_e32 v[66:67], v[16:17]
	v_mov_b64_e32 v[50:51], v[16:17]
	v_mov_b64_e32 v[34:35], v[16:17]
	v_mov_b64_e32 v[128:129], v[14:15]
	v_mov_b64_e32 v[126:127], v[12:13]
	v_mov_b64_e32 v[124:125], v[10:11]
	v_mov_b64_e32 v[122:123], v[8:9]
	v_mov_b64_e32 v[120:121], v[6:7]
	v_mov_b64_e32 v[118:119], v[4:5]
	v_mov_b64_e32 v[116:117], v[2:3]
	v_mov_b64_e32 v[112:113], v[14:15]
	v_mov_b64_e32 v[110:111], v[12:13]
	v_mov_b64_e32 v[108:109], v[10:11]
	v_mov_b64_e32 v[106:107], v[8:9]
	v_mov_b64_e32 v[104:105], v[6:7]
	v_mov_b64_e32 v[102:103], v[4:5]
	v_mov_b64_e32 v[100:101], v[2:3]
	v_mov_b64_e32 v[96:97], v[14:15]
	v_mov_b64_e32 v[94:95], v[12:13]
	v_mov_b64_e32 v[92:93], v[10:11]
	v_mov_b64_e32 v[90:91], v[8:9]
	v_mov_b64_e32 v[88:89], v[6:7]
	v_mov_b64_e32 v[86:87], v[4:5]
	v_mov_b64_e32 v[84:85], v[2:3]
	v_mov_b64_e32 v[80:81], v[14:15]
	v_mov_b64_e32 v[78:79], v[12:13]
	v_mov_b64_e32 v[76:77], v[10:11]
	v_mov_b64_e32 v[74:75], v[8:9]
	v_mov_b64_e32 v[72:73], v[6:7]
	v_mov_b64_e32 v[70:71], v[4:5]
	v_mov_b64_e32 v[68:69], v[2:3]
	v_mov_b64_e32 v[64:65], v[14:15]
	v_mov_b64_e32 v[62:63], v[12:13]
	v_mov_b64_e32 v[60:61], v[10:11]
	v_mov_b64_e32 v[58:59], v[8:9]
	v_mov_b64_e32 v[56:57], v[6:7]
	v_mov_b64_e32 v[54:55], v[4:5]
	v_mov_b64_e32 v[52:53], v[2:3]
	v_mov_b64_e32 v[48:49], v[14:15]
	v_mov_b64_e32 v[46:47], v[12:13]
	v_mov_b64_e32 v[44:45], v[10:11]
	v_mov_b64_e32 v[42:43], v[8:9]
	v_mov_b64_e32 v[40:41], v[6:7]
	v_mov_b64_e32 v[38:39], v[4:5]
	v_mov_b64_e32 v[36:37], v[2:3]
	v_mov_b64_e32 v[32:33], v[14:15]
	v_mov_b64_e32 v[30:31], v[12:13]
	v_mov_b64_e32 v[28:29], v[10:11]
	v_mov_b64_e32 v[26:27], v[8:9]
	v_mov_b64_e32 v[24:25], v[6:7]
	v_mov_b64_e32 v[22:23], v[4:5]
	v_mov_b64_e32 v[20:21], v[2:3]
	v_mov_b64_e32 v[18:19], v[16:17]
	s_mov_b32 s10, 0
	v_lshl_add_u32 v243, v213, 2, v232
	v_mov_b32_e32 v245, 0
	v_mov_b32_e32 v248, 0xf149f2ca
	s_mov_b64 s[82:83], 0
	s_mov_b32 s86, 0x8000
	v_mov_b64_e32 v[16:17], v[14:15]
	v_mov_b64_e32 v[14:15], v[12:13]
	v_mov_b64_e32 v[12:13], v[10:11]
	v_mov_b64_e32 v[10:11], v[8:9]
	v_mov_b64_e32 v[8:9], v[6:7]
	v_mov_b64_e32 v[6:7], v[4:5]
	v_mov_b64_e32 v[4:5], v[2:3]
	s_waitcnt vmcnt(1)
	ds_write_b128 v241, v[204:207] offset:16384
	s_waitcnt vmcnt(0)
	ds_write_b128 v241, v[208:211] offset:18432
	s_waitcnt lgkmcnt(0)
	s_barrier
